# baseline (speedup 1.0000x reference)
.LBB0_19:
	s_and_b64 vcc, exec, s[2:3]
	s_cbranch_vccz .LBB0_114
	s_load_dwordx2 s[4:5], s[0:1], 0x40
	s_load_dwordx2 s[2:3], s[0:1], 0x0
	v_and_b32_e32 v2, 7, v0
	v_lshrrev_b32_e32 v4, 6, v0
	v_bfe_u32 v5, v0, 3, 3
	v_lshl_or_b32 v2, v4, 3, v2
	v_lshl_or_b32 v0, v5, 5, v2
	v_bfe_u32 v1, v0, 3, 2
	v_lshl_or_b32 v2, s26, 10, v0
	v_add_u32_e32 v7, 0xfff9e400, v2
	v_and_b32_e32 v2, 31, v0
	v_lshlrev_b32_e32 v4, 5, v2
	v_mov_b32_e32 v5, 0
	s_waitcnt lgkmcnt(0)
	v_lshl_add_u64 v[2:3], s[2:3], 0, v[4:5]
	v_mul_u32_u24_e32 v6, 0xc350, v1
	v_lshlrev_b32_e32 v1, 4, v0
	s_mov_b32 s2, 0x186a00
	s_mov_b32 s7, 0x20000
	s_mov_b32 s6, 0x186a000
	s_and_b32 s5, s5, 0xffff
	v_and_b32_e32 v1, 0x70, v1
	v_cmp_gt_u32_e32 vcc, s2, v7
	s_and_saveexec_b64 s[2:3], vcc
	s_cbranch_execz .LBB0_22
	v_lshrrev_b32_e32 v16, 5, v7
	v_lshlrev_b32_e32 v4, 10, v16
	v_lshl_add_u64 v[4:5], v[2:3], 0, v[4:5]
	global_load_dwordx4 v[8:11], v[4:5], off offset:16 nt
	global_load_dwordx4 v[12:15], v[4:5], off nt
	v_add_u32_e32 v4, v16, v6
	v_lshl_or_b32 v4, v4, 7, v1
	s_waitcnt vmcnt(1)
	v_cvt_pk_f16_f32 v11, v10, v11
	v_cvt_pk_f16_f32 v10, v8, v9
	s_waitcnt vmcnt(0)
	v_cvt_pk_f16_f32 v9, v14, v15
	v_cvt_pk_f16_f32 v8, v12, v13
	buffer_store_dwordx4 v[8:11], v4, s[4:7], 0 offen sc1
